# baseline (speedup 1.0000x reference)
.Lno_anc:
	s_or_b64 exec, exec, s[8:9]
	v_mov_b32_e32 v7, 0x80
	s_cmp_ge_u32 s2, 8
	s_cbranch_scc1 .Lno_touch
	v_lshlrev_b32_e32 v9, 4, v6
	v_lshl_add_u32 v9, v10, 21, v9
	s_mov_b64 exec, 3
	global_load_dword v24, v9, s[16:17] nt
	global_load_dword v25, v9, s[18:19] nt
	s_mov_b64 exec, -1
	s_waitcnt vmcnt(2)
	s_branch .Lmask_ready
